# select matrix in product form: clamp(c*(S-c)-P) with pk_fma_f16, 2 ops per register instead of 3 (exact f16 integers)
# speedup vs baseline: 1.0012x; 1.0004x over previous
.Lcs_done:
	global_load_dword v241, v4, s[54:55]
	s_add_i32 s18, s13, 32
	s_add_i32 s19, s13, 16
	s_mov_b64 s[6:7], 0
	v_mfma_f32_32x32x16_f16 v[82:97], v[194:197], v[178:181], 0
	v_mfma_f32_32x32x16_f16 v[98:113], v[194:197], v[182:185], 0
	v_add_u32_e32 v14, s13, v243
	v_sub_u32_e32 v3, v230, v14
	v_add_u32_e32 v4, v3, v234
	v_add_u32_e32 v5, -1, v3
	v_med3_i32 v4, v4, -1, 32
	v_med3_i32 v5, v5, -1, 32
	v_cvt_f32_i32_e32 v4, v4
	v_cvt_f32_i32_e32 v5, v5
	v_cvt_pk_f16_f32 v14, v4, v4
	v_cvt_pk_f16_f32 v15, v5, v5
	v_pk_add_f16 v3, v14, v15
	v_pk_mul_f16 v4, v14, v15
	v_pk_add_f16 v5, v3, s73 neg_lo:[0,1] neg_hi:[0,1]
	v_pk_add_f16 v16, v3, s74 neg_lo:[0,1] neg_hi:[0,1]
	v_pk_fma_f16 v6, v5, s73, v4 neg_lo:[0,0,1] neg_hi:[0,0,1] clamp
	v_pk_add_f16 v5, v3, s75 neg_lo:[0,1] neg_hi:[0,1]
	v_pk_fma_f16 v7, v16, s74, v4 neg_lo:[0,0,1] neg_hi:[0,0,1] clamp
	v_pk_add_f16 v16, v3, s76 neg_lo:[0,1] neg_hi:[0,1]
	v_pk_fma_f16 v8, v5, s75, v4 neg_lo:[0,0,1] neg_hi:[0,0,1] clamp
	v_pk_add_f16 v5, v3, s77 neg_lo:[0,1] neg_hi:[0,1]
	v_pk_fma_f16 v9, v16, s76, v4 neg_lo:[0,0,1] neg_hi:[0,0,1] clamp
	v_pk_add_f16 v16, v3, s78 neg_lo:[0,1] neg_hi:[0,1]
	v_pk_fma_f16 v10, v5, s77, v4 neg_lo:[0,0,1] neg_hi:[0,0,1] clamp
	v_pk_add_f16 v5, v3, s79 neg_lo:[0,1] neg_hi:[0,1]
	v_pk_fma_f16 v11, v16, s78, v4 neg_lo:[0,0,1] neg_hi:[0,0,1] clamp
	v_pk_add_f16 v16, v3, s80 neg_lo:[0,1] neg_hi:[0,1]
	v_pk_fma_f16 v12, v5, s79, v4 neg_lo:[0,0,1] neg_hi:[0,0,1] clamp
	v_pk_fma_f16 v13, v16, s80, v4 neg_lo:[0,0,1] neg_hi:[0,0,1] clamp
	v_exp_f32_e32 v82, v82
	v_exp_f32_e32 v83, v83
	v_exp_f32_e32 v84, v84
	v_exp_f32_e32 v85, v85
	v_exp_f32_e32 v86, v86
	v_exp_f32_e32 v87, v87
	v_exp_f32_e32 v88, v88
	v_exp_f32_e32 v89, v89
	v_exp_f32_e32 v90, v90
	v_exp_f32_e32 v91, v91
	v_exp_f32_e32 v92, v92
	v_exp_f32_e32 v93, v93
	v_exp_f32_e32 v94, v94
	v_exp_f32_e32 v95, v95
	v_exp_f32_e32 v96, v96
	v_exp_f32_e32 v97, v97
	v_pk_add_f32 v[82:83], v[82:83], s[82:83]
	v_pk_add_f32 v[84:85], v[84:85], s[82:83]
	v_pk_add_f32 v[86:87], v[86:87], s[82:83]
	v_pk_add_f32 v[88:89], v[88:89], s[82:83]
	v_pk_add_f32 v[90:91], v[90:91], s[82:83]
	v_pk_add_f32 v[92:93], v[92:93], s[82:83]
	v_pk_add_f32 v[94:95], v[94:95], s[82:83]
	v_pk_add_f32 v[96:97], v[96:97], s[82:83]
	v_rcp_f32_e32 v82, v82
	v_rcp_f32_e32 v83, v83
	v_rcp_f32_e32 v84, v84
	v_rcp_f32_e32 v85, v85
	v_rcp_f32_e32 v86, v86
	v_rcp_f32_e32 v87, v87
	v_rcp_f32_e32 v88, v88
	v_rcp_f32_e32 v89, v89
	v_rcp_f32_e32 v90, v90
	v_rcp_f32_e32 v91, v91
	v_rcp_f32_e32 v92, v92
	v_rcp_f32_e32 v93, v93
	v_rcp_f32_e32 v94, v94
	v_rcp_f32_e32 v95, v95
	v_rcp_f32_e32 v96, v96
	v_rcp_f32_e32 v97, v97
	v_cvt_pk_f16_f32 v198, v82, v83
	v_cvt_pk_f16_f32 v199, v84, v85
	v_cvt_pk_f16_f32 v200, v86, v87
	v_cvt_pk_f16_f32 v201, v88, v89
	v_cvt_pk_f16_f32 v202, v90, v91
	v_cvt_pk_f16_f32 v203, v92, v93
	v_cvt_pk_f16_f32 v204, v94, v95
	v_cvt_pk_f16_f32 v205, v96, v97
	v_mfma_f32_32x32x16_f16 v[82:97], v[194:197], v[186:189], 0
	v_exp_f32_e32 v98, v98
	v_exp_f32_e32 v99, v99
	v_exp_f32_e32 v100, v100
	v_exp_f32_e32 v101, v101
	v_exp_f32_e32 v102, v102
	v_exp_f32_e32 v103, v103
	v_mfma_f32_32x32x16_f16 v[66:81], v[198:201], v[6:9], v[66:81]
	v_exp_f32_e32 v104, v104
	v_exp_f32_e32 v105, v105
	v_exp_f32_e32 v106, v106
	v_exp_f32_e32 v107, v107
	v_exp_f32_e32 v108, v108
	v_exp_f32_e32 v109, v109
	v_mfma_f32_32x32x16_f16 v[66:81], v[202:205], v[10:13], v[66:81]
	v_exp_f32_e32 v110, v110
	v_exp_f32_e32 v111, v111
	v_exp_f32_e32 v112, v112
	v_exp_f32_e32 v113, v113
	v_pk_add_f32 v[98:99], v[98:99], s[82:83]
	v_pk_add_f32 v[100:101], v[100:101], s[82:83]
	v_pk_add_f32 v[102:103], v[102:103], s[82:83]
	v_pk_add_f32 v[104:105], v[104:105], s[82:83]
	v_pk_add_f32 v[106:107], v[106:107], s[82:83]
	v_pk_add_f32 v[108:109], v[108:109], s[82:83]
	v_pk_add_f32 v[110:111], v[110:111], s[82:83]
	v_pk_add_f32 v[112:113], v[112:113], s[82:83]
	v_rcp_f32_e32 v98, v98
	v_rcp_f32_e32 v99, v99
	v_rcp_f32_e32 v100, v100
	v_rcp_f32_e32 v101, v101
	v_rcp_f32_e32 v102, v102
	v_rcp_f32_e32 v103, v103
	v_rcp_f32_e32 v104, v104
	v_rcp_f32_e32 v105, v105
	v_rcp_f32_e32 v106, v106
	v_rcp_f32_e32 v107, v107
	v_rcp_f32_e32 v108, v108
	v_rcp_f32_e32 v109, v109
	v_rcp_f32_e32 v110, v110
	v_rcp_f32_e32 v111, v111
	v_rcp_f32_e32 v112, v112
	v_rcp_f32_e32 v113, v113
	v_cvt_pk_f16_f32 v206, v98, v99
	v_cvt_pk_f16_f32 v207, v100, v101
	v_cvt_pk_f16_f32 v208, v102, v103
	v_cvt_pk_f16_f32 v209, v104, v105
	v_cvt_pk_f16_f32 v210, v106, v107
	v_cvt_pk_f16_f32 v211, v108, v109
	v_cvt_pk_f16_f32 v212, v110, v111
	v_cvt_pk_f16_f32 v213, v112, v113
	v_mfma_f32_32x32x16_f16 v[98:113], v[194:197], v[190:193], 0
	v_exp_f32_e32 v82, v82
	v_exp_f32_e32 v83, v83
	v_exp_f32_e32 v84, v84
	v_exp_f32_e32 v85, v85
	v_exp_f32_e32 v86, v86
	v_exp_f32_e32 v87, v87
	v_mfma_f32_32x32x16_f16 v[50:65], v[206:209], v[6:9], v[50:65]
	v_exp_f32_e32 v88, v88
	v_exp_f32_e32 v89, v89
	v_exp_f32_e32 v90, v90
	v_exp_f32_e32 v91, v91
	v_exp_f32_e32 v92, v92
	v_exp_f32_e32 v93, v93
	v_mfma_f32_32x32x16_f16 v[50:65], v[210:213], v[10:13], v[50:65]
	v_exp_f32_e32 v94, v94
	v_exp_f32_e32 v95, v95
	v_exp_f32_e32 v96, v96
	v_exp_f32_e32 v97, v97
	v_pk_add_f32 v[82:83], v[82:83], s[82:83]
	v_pk_add_f32 v[84:85], v[84:85], s[82:83]
	v_pk_add_f32 v[86:87], v[86:87], s[82:83]
	v_pk_add_f32 v[88:89], v[88:89], s[82:83]
	v_pk_add_f32 v[90:91], v[90:91], s[82:83]
	v_pk_add_f32 v[92:93], v[92:93], s[82:83]
	v_pk_add_f32 v[94:95], v[94:95], s[82:83]
	v_pk_add_f32 v[96:97], v[96:97], s[82:83]
	v_rcp_f32_e32 v82, v82
	v_rcp_f32_e32 v83, v83
	v_rcp_f32_e32 v84, v84
	v_rcp_f32_e32 v85, v85
	v_rcp_f32_e32 v86, v86
	v_rcp_f32_e32 v87, v87
	v_rcp_f32_e32 v88, v88
	v_rcp_f32_e32 v89, v89
	v_rcp_f32_e32 v90, v90
	v_rcp_f32_e32 v91, v91
	v_rcp_f32_e32 v92, v92
	v_rcp_f32_e32 v93, v93
	v_rcp_f32_e32 v94, v94
	v_rcp_f32_e32 v95, v95
	v_rcp_f32_e32 v96, v96
	v_rcp_f32_e32 v97, v97
	v_cvt_pk_f16_f32 v214, v82, v83
	v_cvt_pk_f16_f32 v215, v84, v85
	v_cvt_pk_f16_f32 v216, v86, v87
	v_cvt_pk_f16_f32 v217, v88, v89
	v_cvt_pk_f16_f32 v218, v90, v91
	v_cvt_pk_f16_f32 v219, v92, v93
	v_cvt_pk_f16_f32 v220, v94, v95
	v_cvt_pk_f16_f32 v221, v96, v97
	v_exp_f32_e32 v98, v98
	v_exp_f32_e32 v99, v99
	v_exp_f32_e32 v100, v100
	v_exp_f32_e32 v101, v101
	v_exp_f32_e32 v102, v102
	v_exp_f32_e32 v103, v103
	v_mfma_f32_32x32x16_f16 v[34:49], v[214:217], v[6:9], v[34:49]
	v_exp_f32_e32 v104, v104
	v_exp_f32_e32 v105, v105
	v_exp_f32_e32 v106, v106
	v_exp_f32_e32 v107, v107
	v_exp_f32_e32 v108, v108
	v_exp_f32_e32 v109, v109
	v_mfma_f32_32x32x16_f16 v[34:49], v[218:221], v[10:13], v[34:49]
	v_exp_f32_e32 v110, v110
	v_exp_f32_e32 v111, v111
	v_exp_f32_e32 v112, v112
	v_exp_f32_e32 v113, v113
	v_pk_add_f32 v[98:99], v[98:99], s[82:83]
	v_pk_add_f32 v[100:101], v[100:101], s[82:83]
	v_pk_add_f32 v[102:103], v[102:103], s[82:83]
	v_pk_add_f32 v[104:105], v[104:105], s[82:83]
	v_pk_add_f32 v[106:107], v[106:107], s[82:83]
	v_pk_add_f32 v[108:109], v[108:109], s[82:83]
	v_pk_add_f32 v[110:111], v[110:111], s[82:83]
	v_pk_add_f32 v[112:113], v[112:113], s[82:83]
	v_rcp_f32_e32 v98, v98
	v_rcp_f32_e32 v99, v99
	v_rcp_f32_e32 v100, v100
	v_rcp_f32_e32 v101, v101
	v_rcp_f32_e32 v102, v102
	v_rcp_f32_e32 v103, v103
	v_rcp_f32_e32 v104, v104
	v_rcp_f32_e32 v105, v105
	v_rcp_f32_e32 v106, v106
	v_rcp_f32_e32 v107, v107
	v_rcp_f32_e32 v108, v108
	v_rcp_f32_e32 v109, v109
	v_rcp_f32_e32 v110, v110
	v_rcp_f32_e32 v111, v111
	v_rcp_f32_e32 v112, v112
	v_rcp_f32_e32 v113, v113
	v_cvt_pk_f16_f32 v222, v98, v99
	v_cvt_pk_f16_f32 v223, v100, v101
	v_cvt_pk_f16_f32 v224, v102, v103
	v_cvt_pk_f16_f32 v225, v104, v105
	v_cvt_pk_f16_f32 v226, v106, v107
	v_cvt_pk_f16_f32 v227, v108, v109
	v_cvt_pk_f16_f32 v228, v110, v111
	v_cvt_pk_f16_f32 v229, v112, v113
	v_mfma_f32_32x32x16_f16 v[18:33], v[222:225], v[6:9], v[18:33]
	v_add_u32_e32 v194, s13, v243
	v_mfma_f32_32x32x16_f16 v[18:33], v[226:229], v[10:13], v[18:33]
	s_cmp_ge_i32 s18, s71
	s_cbranch_scc1 .Lflush

.LBB1_149:
	v_sub_u32_e32 v3, v230, v194
	s_waitcnt lgkmcnt(0)
	v_add_u32_e32 v4, v3, v234
	v_add_u32_e32 v5, -1, v3
	v_med3_i32 v4, v4, -1, 32
	v_med3_i32 v5, v5, -1, 32
	v_cvt_f32_i32_e32 v4, v4
	v_cvt_f32_i32_e32 v5, v5
	v_cvt_pk_f16_f32 v14, v4, v4
	v_cvt_pk_f16_f32 v15, v5, v5
	v_pk_add_f16 v3, v14, v15
	v_pk_mul_f16 v4, v14, v15
	v_pk_add_f16 v5, v3, s73 neg_lo:[0,1] neg_hi:[0,1]
	v_pk_add_f16 v16, v3, s74 neg_lo:[0,1] neg_hi:[0,1]
	v_pk_fma_f16 v6, v5, s73, v4 neg_lo:[0,0,1] neg_hi:[0,0,1] clamp
	v_pk_add_f16 v5, v3, s75 neg_lo:[0,1] neg_hi:[0,1]
	v_pk_fma_f16 v7, v16, s74, v4 neg_lo:[0,0,1] neg_hi:[0,0,1] clamp
	v_pk_add_f16 v16, v3, s76 neg_lo:[0,1] neg_hi:[0,1]
	v_pk_fma_f16 v8, v5, s75, v4 neg_lo:[0,0,1] neg_hi:[0,0,1] clamp
	v_pk_fma_f16 v9, v16, s76, v4 neg_lo:[0,0,1] neg_hi:[0,0,1] clamp
	s_nop 1
	v_mfma_f32_32x32x16_f16 v[66:81], v[198:201], v[6:9], 0
	v_mfma_f32_32x32x16_f16 v[50:65], v[206:209], v[6:9], 0
	v_mfma_f32_32x32x16_f16 v[34:49], v[214:217], v[6:9], 0
	v_mfma_f32_32x32x16_f16 v[18:33], v[222:225], v[6:9], 0
.LBB1_151:
	s_cmp_le_i32 s18, s70
	s_cbranch_scc1 .LBB1_153
	s_cmp_ge_i32 s19, s71
	s_cbranch_scc1 .LBB1_153
	v_pk_add_f16 v5, v3, s77 neg_lo:[0,1] neg_hi:[0,1]
	v_pk_add_f16 v16, v3, s78 neg_lo:[0,1] neg_hi:[0,1]
	v_pk_fma_f16 v6, v5, s77, v4 neg_lo:[0,0,1] neg_hi:[0,0,1] clamp
	v_pk_add_f16 v5, v3, s79 neg_lo:[0,1] neg_hi:[0,1]
	v_pk_fma_f16 v7, v16, s78, v4 neg_lo:[0,0,1] neg_hi:[0,0,1] clamp
	v_pk_add_f16 v16, v3, s80 neg_lo:[0,1] neg_hi:[0,1]
	v_pk_fma_f16 v8, v5, s79, v4 neg_lo:[0,0,1] neg_hi:[0,0,1] clamp
	v_pk_fma_f16 v9, v16, s80, v4 neg_lo:[0,0,1] neg_hi:[0,0,1] clamp
	s_nop 1
	v_mfma_f32_32x32x16_f16 v[66:81], v[202:205], v[6:9], v[66:81]
	v_mfma_f32_32x32x16_f16 v[50:65], v[210:213], v[6:9], v[50:65]
	v_mfma_f32_32x32x16_f16 v[34:49], v[218:221], v[6:9], v[34:49]
	v_mfma_f32_32x32x16_f16 v[18:33], v[226:229], v[6:9], v[18:33]
